# MoE start-up (DPP prefix table, shift/ballot first-unit decode) + gMLP spatial-weight quads prefetched at unit top
# speedup vs baseline: 1.0322x; 1.0010x over previous
.LBB0_1216:
	s_mov_b32 s0, 4
	s_ashr_i32 s1, s0, 31
	s_lshl_b64 s[0:1], s[0:1], 3
	s_add_u32 s0, s94, s0
	s_addc_u32 s1, s95, s1
	s_load_dwordx2 s[0:1], s[0:1], 0x0
	v_mov_b32_e32 v19, v0
	v_mov_b64_e32 v[6:7], s[28:29]
	s_waitcnt lgkmcnt(0)
	s_add_u32 s12, s0, s4
	s_mov_b32 s0, 5
	s_addc_u32 s13, s1, s5
	s_ashr_i32 s1, s0, 31
	s_lshl_b64 s[0:1], s[0:1], 3
	s_add_u32 s0, s94, s0
	s_addc_u32 s1, s95, s1
	s_load_dwordx2 s[8:9], s[0:1], 0x0
	s_mov_b32 s0, 6
	s_ashr_i32 s1, s0, 31
	s_lshl_b64 s[0:1], s[0:1], 3
	s_add_u32 s0, s94, s0
	s_addc_u32 s1, s95, s1
	s_load_dwordx2 s[10:11], s[0:1], 0x0
	s_and_b32 s21, s16, 0xffffff80
	v_ashrrev_i32_e32 v5, 2, v19
	v_lshlrev_b32_e32 v1, 5, v19
	v_and_b32_e32 v4, 0x60, v1
	v_add_u32_e32 v1, s21, v5
	v_mad_i64_i32 v[6:7], s[0:1], v1, s96, v[6:7]
	s_and_b32 s72, s18, 0x180
	s_lshl_b32 s0, s72, 1
	s_mov_b32 s1, s73
	v_lshl_add_u64 v[6:7], v[6:7], 0, s[0:1]
	v_lshlrev_b32_e32 v2, 1, v4
	v_lshl_add_u64 v[14:15], v[6:7], 0, v[2:3]
	global_load_dwordx4 v[40:43], v[14:15], off offset:1072
	global_load_dwordx4 v[6:9], v[14:15], off offset:1056
	global_load_dwordx4 v[10:13], v[14:15], off offset:1040
	s_nop 0
	global_load_dwordx4 v[14:17], v[14:15], off offset:1024
	v_readfirstlane_b32 s100, v19
	s_ashr_i32 s100, s100, 2
	v_bfi_b32 v120, -16, s100, v19
	v_ashrrev_i32_e32 v121, 31, v120
	v_lshl_add_u64 v[120:121], v[120:121], 0, s[72:73]
	v_lshlrev_b64 v[120:121], 9, v[120:121]
	v_lshl_add_u64 v[120:121], s[12:13], 0, v[120:121]
	v_bfe_u32 v122, v19, 4, 2
	v_lshlrev_b32_e32 v122, 5, v122
	v_mov_b32_e32 v123, 0
	v_lshl_add_u64 v[120:121], v[120:121], 0, v[122:123]
	global_load_dwordx4 v[124:127], v[120:121], off
	global_load_dwordx4 v[128:131], v[120:121], off offset:16
	global_load_dwordx4 v[132:135], v[120:121], off offset:128
	global_load_dwordx4 v[136:139], v[120:121], off offset:144
	global_load_dwordx4 v[140:143], v[120:121], off offset:256
	global_load_dwordx4 v[144:147], v[120:121], off offset:272
	global_load_dwordx4 v[148:151], v[120:121], off offset:384
	global_load_dwordx4 v[152:155], v[120:121], off offset:400
	v_lshlrev_b32_e32 v5, 1, v5
	v_mul_u32_u24_e32 v4, 0x110, v4
	v_add3_u32 v4, 0, v4, v5
	v_bfe_u32 v47, v19, 4, 2
	v_and_b32_e32 v46, 15, v19
	v_lshlrev_b32_e32 v48, 3, v47
	v_lshlrev_b32_e32 v44, 2, v48
	s_waitcnt vmcnt(10)
	v_lshlrev_b32_e32 v24, 16, v6
	s_waitcnt vmcnt(9)
	v_and_b32_e32 v27, 0xffff0000, v10
	s_waitcnt vmcnt(8)
	v_and_b32_e32 v36, 0xffff0000, v14
	v_and_b32_e32 v33, 0xffff0000, v15
	v_lshlrev_b32_e32 v38, 16, v14
	v_mul_f32_e32 v1, v36, v36
	v_lshlrev_b32_e32 v37, 16, v15
	v_mul_f32_e32 v2, v33, v33
	v_fmac_f32_e32 v1, v38, v38
	v_fmac_f32_e32 v2, v37, v37
	v_and_b32_e32 v31, 0xffff0000, v16
	v_add_f32_e32 v1, v1, v2
	v_lshlrev_b32_e32 v35, 16, v16
	v_mul_f32_e32 v2, v31, v31
	v_fmac_f32_e32 v2, v35, v35
	v_and_b32_e32 v29, 0xffff0000, v17
	v_add_f32_e32 v1, v2, v1
	v_lshlrev_b32_e32 v34, 16, v17
	v_mul_f32_e32 v2, v29, v29
	v_fmac_f32_e32 v2, v34, v34
	v_add_f32_e32 v1, v2, v1
	v_lshlrev_b32_e32 v32, 16, v10
	v_mul_f32_e32 v2, v27, v27
	v_fmac_f32_e32 v2, v32, v32
	v_and_b32_e32 v25, 0xffff0000, v11
	v_add_f32_e32 v1, v2, v1
	v_lshlrev_b32_e32 v30, 16, v11
	v_mul_f32_e32 v2, v25, v25
	v_fmac_f32_e32 v2, v30, v30
	v_and_b32_e32 v23, 0xffff0000, v12
	v_add_f32_e32 v1, v2, v1
	v_lshlrev_b32_e32 v28, 16, v12
	v_mul_f32_e32 v2, v23, v23
	v_fmac_f32_e32 v2, v28, v28
	v_and_b32_e32 v21, 0xffff0000, v13
	v_add_f32_e32 v1, v2, v1
	v_lshlrev_b32_e32 v26, 16, v13
	v_mul_f32_e32 v2, v21, v21
	v_fmac_f32_e32 v2, v26, v26
	v_and_b32_e32 v17, 0xffff0000, v6
	v_add_f32_e32 v1, v2, v1
	v_mul_f32_e32 v2, v17, v17
	v_fmac_f32_e32 v2, v24, v24
	v_and_b32_e32 v15, 0xffff0000, v7
	v_add_f32_e32 v1, v2, v1
	v_lshlrev_b32_e32 v22, 16, v7
	v_mul_f32_e32 v2, v15, v15
	v_fmac_f32_e32 v2, v22, v22
	v_and_b32_e32 v13, 0xffff0000, v8
	v_add_f32_e32 v1, v2, v1
	v_lshlrev_b32_e32 v20, 16, v8
	v_mul_f32_e32 v2, v13, v13
	v_fmac_f32_e32 v2, v20, v20
	v_and_b32_e32 v11, 0xffff0000, v9
	v_add_f32_e32 v1, v2, v1
	v_lshlrev_b32_e32 v16, 16, v9
	v_mul_f32_e32 v2, v11, v11
	v_fmac_f32_e32 v2, v16, v16
	v_and_b32_e32 v9, 0xffff0000, v40
	v_add_f32_e32 v1, v2, v1
	v_lshlrev_b32_e32 v14, 16, v40
	v_mul_f32_e32 v2, v9, v9
	v_fmac_f32_e32 v2, v14, v14
	v_and_b32_e32 v7, 0xffff0000, v41
	v_add_f32_e32 v1, v2, v1
	v_lshlrev_b32_e32 v12, 16, v41
	v_mul_f32_e32 v2, v7, v7
	v_fmac_f32_e32 v2, v12, v12
	v_and_b32_e32 v6, 0xffff0000, v42
	v_add_f32_e32 v1, v2, v1
	v_lshlrev_b32_e32 v10, 16, v42
	v_mul_f32_e32 v2, v6, v6
	v_fmac_f32_e32 v2, v10, v10
	v_add_f32_e32 v1, v2, v1
	v_and_b32_e32 v2, 0xffff0000, v43
	v_lshlrev_b32_e32 v8, 16, v43
	v_mul_f32_e32 v39, v2, v2
	v_fmac_f32_e32 v39, v8, v8
	v_and_b32_e32 v40, 64, v222
	v_add_f32_e32 v39, v39, v1
	v_xor_b32_e32 v1, 1, v222
	v_add_u32_e32 v40, 64, v40
	v_cmp_lt_i32_e32 vcc, v1, v40
	s_nop 1
	v_cndmask_b32_e32 v1, v222, v1, vcc
	v_lshlrev_b32_e32 v1, 2, v1
	ds_bpermute_b32 v1, v1, v39
	s_waitcnt lgkmcnt(0)
	v_add_f32_e32 v1, v39, v1
	v_xor_b32_e32 v39, 2, v222
	v_cmp_lt_i32_e32 vcc, v39, v40
	s_nop 1
	v_cndmask_b32_e32 v39, v222, v39, vcc
	v_lshlrev_b32_e32 v39, 2, v39
	ds_bpermute_b32 v39, v39, v1
	s_waitcnt lgkmcnt(0)
	v_add_f32_e32 v1, v1, v39
	v_fmamk_f32 v1, v1, 0x3c000000, v220
	v_cmp_gt_f32_e32 vcc, s93, v1
	v_mul_f32_e32 v39, 0x4f800000, v1
	s_nop 0
	v_cndmask_b32_e32 v1, v1, v39, vcc
	v_sqrt_f32_e32 v39, v1
	s_nop 0
	v_add_u32_e32 v40, -1, v39
	v_fma_f32 v41, -v40, v39, v1
	v_cmp_ge_f32_e64 s[0:1], 0, v41
	v_add_u32_e32 v41, 1, v39
	s_nop 0
	v_cndmask_b32_e64 v40, v39, v40, s[0:1]
	v_fma_f32 v39, -v41, v39, v1
	v_cmp_lt_f32_e64 s[0:1], 0, v39
	s_nop 1
	v_cndmask_b32_e64 v39, v40, v41, s[0:1]
	v_mul_f32_e32 v40, 0x37800000, v39
	v_cndmask_b32_e32 v39, v39, v40, vcc
	v_cmp_class_f32_e32 vcc, v1, v221
	s_nop 1
	v_cndmask_b32_e32 v1, v39, v1, vcc
	v_div_scale_f32 v39, s[0:1], v1, v1, 1.0
	v_rcp_f32_e32 v40, v39
	v_readfirstlane_b32 s0, v19
	s_ashr_i32 s0, s0, 2
	s_cmp_lt_i32 s0, 0
	v_fma_f32 v41, -v39, v40, 1.0
	v_fmac_f32_e32 v40, v41, v40
	v_div_scale_f32 v41, vcc, 1.0, v1, 1.0
	v_mul_f32_e32 v42, v41, v40
	v_fma_f32 v43, -v39, v42, v41
	v_fmac_f32_e32 v42, v43, v40
	v_fma_f32 v39, -v39, v42, v41
	v_div_fmas_f32 v39, v39, v40, v42
	v_div_fixup_f32 v1, v39, v1, 1.0
	v_mul_f32_e32 v38, v1, v38
	v_mul_f32_e32 v5, v1, v36
	v_cvt_pk_bf16_f32 v38, v38, v3
	ds_write_b16 v4, v38
	v_cvt_pk_bf16_f32 v5, v5, v3
	ds_write_b16 v4, v5 offset:272
	v_mul_f32_e32 v5, v1, v37
	v_cvt_pk_bf16_f32 v5, v5, v3
	ds_write_b16 v4, v5 offset:544
	v_mul_f32_e32 v5, v1, v33
	v_cvt_pk_bf16_f32 v5, v5, v3
	ds_write_b16 v4, v5 offset:816
	v_mul_f32_e32 v5, v1, v35
	v_cvt_pk_bf16_f32 v5, v5, v3
	ds_write_b16 v4, v5 offset:1088
	v_mul_f32_e32 v5, v1, v31
	v_cvt_pk_bf16_f32 v5, v5, v3
	ds_write_b16 v4, v5 offset:1360
	v_mul_f32_e32 v5, v1, v34
	v_cvt_pk_bf16_f32 v5, v5, v3
	ds_write_b16 v4, v5 offset:1632
	v_mul_f32_e32 v5, v1, v29
	v_cvt_pk_bf16_f32 v5, v5, v3
	ds_write_b16 v4, v5 offset:1904
	v_mul_f32_e32 v5, v1, v32
	v_cvt_pk_bf16_f32 v5, v5, v3
	ds_write_b16 v4, v5 offset:2176
	v_mul_f32_e32 v5, v1, v27
	v_cvt_pk_bf16_f32 v5, v5, v3
	ds_write_b16 v4, v5 offset:2448
	v_mul_f32_e32 v5, v1, v30
	v_cvt_pk_bf16_f32 v5, v5, v3
	ds_write_b16 v4, v5 offset:2720
	v_mul_f32_e32 v5, v1, v25
	v_cvt_pk_bf16_f32 v5, v5, v3
	ds_write_b16 v4, v5 offset:2992
	v_mul_f32_e32 v5, v1, v28
	v_cvt_pk_bf16_f32 v5, v5, v3
	ds_write_b16 v4, v5 offset:3264
	v_mul_f32_e32 v5, v1, v23
	v_cvt_pk_bf16_f32 v5, v5, v3
	ds_write_b16 v4, v5 offset:3536
	v_mul_f32_e32 v5, v1, v26
	v_cvt_pk_bf16_f32 v5, v5, v3
	ds_write_b16 v4, v5 offset:3808
	v_mul_f32_e32 v5, v1, v21
	v_cvt_pk_bf16_f32 v5, v5, v3
	ds_write_b16 v4, v5 offset:4080
	v_mul_f32_e32 v5, v1, v24
	v_cvt_pk_bf16_f32 v5, v5, v3
	ds_write_b16 v4, v5 offset:4352
	v_mul_f32_e32 v5, v1, v17
	v_cvt_pk_bf16_f32 v5, v5, v3
	ds_write_b16 v4, v5 offset:4624
	v_mul_f32_e32 v5, v1, v22
	v_cvt_pk_bf16_f32 v5, v5, v3
	ds_write_b16 v4, v5 offset:4896
	v_mul_f32_e32 v5, v1, v15
	v_cvt_pk_bf16_f32 v5, v5, v3
	ds_write_b16 v4, v5 offset:5168
	v_mul_f32_e32 v5, v1, v20
	v_cvt_pk_bf16_f32 v5, v5, v3
	ds_write_b16 v4, v5 offset:5440
	v_mul_f32_e32 v5, v1, v13
	v_cvt_pk_bf16_f32 v5, v5, v3
	ds_write_b16 v4, v5 offset:5712
	v_mul_f32_e32 v5, v1, v16
	v_cvt_pk_bf16_f32 v5, v5, v3
	ds_write_b16 v4, v5 offset:5984
	v_mul_f32_e32 v5, v1, v11
	v_cvt_pk_bf16_f32 v5, v5, v3
	ds_write_b16 v4, v5 offset:6256
	v_mul_f32_e32 v5, v1, v14
	v_cvt_pk_bf16_f32 v5, v5, v3
	ds_write_b16 v4, v5 offset:6528
	v_mul_f32_e32 v5, v1, v9
	v_cvt_pk_bf16_f32 v5, v5, v3
	ds_write_b16 v4, v5 offset:6800
	v_mul_f32_e32 v5, v1, v12
	v_cvt_pk_bf16_f32 v5, v5, v3
	ds_write_b16 v4, v5 offset:7072
	v_mul_f32_e32 v5, v1, v7
	v_cvt_pk_bf16_f32 v5, v5, v3
	ds_write_b16 v4, v5 offset:7344
	v_mul_f32_e32 v5, v1, v10
	v_cvt_pk_bf16_f32 v5, v5, v3
	ds_write_b16 v4, v5 offset:7616
	v_mul_f32_e32 v5, v1, v6
	v_cvt_pk_bf16_f32 v5, v5, v3
	ds_write_b16 v4, v5 offset:7888
	v_mul_f32_e32 v5, v1, v8
	v_bfi_b32 v40, -16, s0, v19
	v_cvt_pk_bf16_f32 v5, v5, v3
	v_mul_f32_e32 v1, v1, v2
	v_ashrrev_i32_e32 v41, 31, v40
	ds_write_b16 v4, v5 offset:8160
	v_cvt_pk_bf16_f32 v1, v1, v3
	ds_write_b16 v4, v1 offset:8432
	v_lshl_add_u64 v[4:5], v[40:41], 0, s[72:73]
	v_lshlrev_b64 v[4:5], 9, v[4:5]
	v_lshl_add_u64 v[42:43], s[12:13], 0, v[4:5]
	v_mul_u32_u24_e32 v41, 0x110, v46
	s_waitcnt lgkmcnt(0)
	s_barrier
	s_cbranch_scc1 .LBB0_1218
	v_mov_b32_e32 v45, v3
	v_lshl_add_u64 v[8:9], v[42:43], 0, v[44:45]
	s_waitcnt vmcnt(0)
	v_mov_b64_e32 v[4:5], v[124:125]
	v_mov_b64_e32 v[6:7], v[126:127]
	s_nop 0
	v_mov_b64_e32 v[8:9], v[128:129]
	v_mov_b64_e32 v[10:11], v[130:131]
	v_cmp_le_i32_e32 vcc, v48, v40
	v_or_b32_e32 v1, 2, v48
	v_or_b32_e32 v2, 3, v48
	v_or_b32_e32 v12, 4, v48
	v_or_b32_e32 v13, 5, v48
	v_or_b32_e32 v14, 6, v48
	v_or_b32_e32 v15, 7, v48
	v_lshlrev_b32_e32 v16, 4, v47
	v_add3_u32 v45, 0, v16, v41
	s_waitcnt vmcnt(1)
	v_cndmask_b32_e32 v4, 0, v4, vcc
	v_cmp_lt_i32_e32 vcc, v48, v40
	s_nop 1
	v_cndmask_b32_e32 v5, 0, v5, vcc
	v_cmp_le_i32_e32 vcc, v1, v40
	v_cvt_pk_bf16_f32 v4, v4, v5
	s_nop 1
	v_cndmask_b32_e32 v1, 0, v6, vcc
	v_cmp_le_i32_e32 vcc, v2, v40
	s_nop 1
	v_cndmask_b32_e32 v2, 0, v7, vcc
	v_cmp_le_i32_e32 vcc, v12, v40
	v_cvt_pk_bf16_f32 v5, v1, v2
	s_waitcnt vmcnt(0)
	s_nop 0
	v_cndmask_b32_e32 v6, 0, v8, vcc
	v_cmp_le_i32_e32 vcc, v13, v40
	s_nop 1
	v_cndmask_b32_e32 v7, 0, v9, vcc
	v_cmp_le_i32_e32 vcc, v14, v40
	v_cvt_pk_bf16_f32 v6, v6, v7
	s_nop 1
	v_cndmask_b32_e32 v8, 0, v10, vcc
	v_cmp_le_i32_e32 vcc, v15, v40
	s_nop 1
	v_cndmask_b32_e32 v9, 0, v11, vcc
	v_cvt_pk_bf16_f32 v7, v8, v9
	ds_read_b128 v[8:11], v45
	ds_read_b128 v[12:15], v45 offset:4352
	s_waitcnt lgkmcnt(1)
	v_mfma_f32_16x16x32_bf16 v[36:39], v[4:7], v[8:11], 0
	s_waitcnt lgkmcnt(0)
	v_mfma_f32_16x16x32_bf16 v[32:35], v[4:7], v[12:15], 0
	ds_read_b128 v[8:11], v45 offset:8704
	ds_read_b128 v[12:15], v45 offset:13056
	s_waitcnt lgkmcnt(1)
	v_mfma_f32_16x16x32_bf16 v[28:31], v[4:7], v[8:11], 0
	s_waitcnt lgkmcnt(0)
	v_mfma_f32_16x16x32_bf16 v[24:27], v[4:7], v[12:15], 0
	ds_read_b128 v[8:11], v45 offset:17408
	ds_read_b128 v[12:15], v45 offset:21760
	s_waitcnt lgkmcnt(1)
	v_mfma_f32_16x16x32_bf16 v[20:23], v[4:7], v[8:11], 0
	ds_read_b128 v[8:11], v45 offset:26112
	ds_read_b128 v[50:53], v45 offset:30464
	s_waitcnt lgkmcnt(2)
	v_mfma_f32_16x16x32_bf16 v[14:17], v[4:7], v[12:15], 0
	s_waitcnt lgkmcnt(1)
	v_mfma_f32_16x16x32_bf16 v[10:13], v[4:7], v[8:11], 0
	s_waitcnt lgkmcnt(0)
	v_mfma_f32_16x16x32_bf16 v[6:9], v[4:7], v[50:53], 0
	s_or_b32 s1, s0, 15
	s_cmp_lt_i32 s1, 32
	s_cbranch_scc0 .LBB0_1219
	s_branch .LBB0_1220

.LBB0_1219:
	v_mov_b32_e32 v45, v3
	v_lshl_add_u64 v[4:5], v[42:43], 0, v[44:45]
	s_waitcnt vmcnt(0)
	v_mov_b64_e32 v[50:51], v[136:137]
	v_mov_b64_e32 v[52:53], v[138:139]
	v_mov_b64_e32 v[54:55], v[132:133]
	v_mov_b64_e32 v[56:57], v[134:135]
	v_or_b32_e32 v1, 32, v48
	v_cmp_le_i32_e32 vcc, v1, v40
	v_or_b32_e32 v4, 33, v48
	v_or_b32_e32 v5, 34, v48
	v_or_b32_e32 v45, 35, v48
	v_or_b32_e32 v49, 36, v48
	v_lshlrev_b32_e32 v1, 1, v1
	v_add3_u32 v1, 0, v1, v41
	s_waitcnt vmcnt(0)
	v_cndmask_b32_e32 v2, 0, v54, vcc
	v_cmp_le_i32_e32 vcc, v4, v40
	s_nop 1
	v_cndmask_b32_e32 v4, 0, v55, vcc
	v_cmp_le_i32_e32 vcc, v5, v40
	s_nop 1
	v_cndmask_b32_e32 v5, 0, v56, vcc
	v_cmp_le_i32_e32 vcc, v45, v40
	s_nop 1
	v_cndmask_b32_e32 v45, 0, v57, vcc
	v_cmp_le_i32_e32 vcc, v49, v40
	s_nop 1
	v_cndmask_b32_e32 v49, 0, v50, vcc
	v_or_b32_e32 v50, 37, v48
	v_cmp_le_i32_e32 vcc, v50, v40
	v_or_b32_e32 v50, 38, v48
	s_nop 0
	v_cndmask_b32_e32 v54, 0, v51, vcc
	v_cmp_le_i32_e32 vcc, v50, v40
	v_or_b32_e32 v50, 39, v48
	s_nop 0
	v_cndmask_b32_e32 v55, 0, v52, vcc
	v_cmp_le_i32_e32 vcc, v50, v40
	v_cvt_pk_bf16_f32 v50, v2, v4
	v_cvt_pk_bf16_f32 v51, v5, v45
	v_cvt_pk_bf16_f32 v52, v49, v54
	s_nop 1
	v_cndmask_b32_e32 v53, 0, v53, vcc
	v_cvt_pk_bf16_f32 v53, v55, v53
	ds_read_b128 v[54:57], v1
	s_waitcnt lgkmcnt(0)
	v_mfma_f32_16x16x32_bf16 v[36:39], v[50:53], v[54:57], v[36:39]
	ds_read_b128 v[54:57], v1 offset:4352
	s_waitcnt lgkmcnt(0)
	v_mfma_f32_16x16x32_bf16 v[32:35], v[50:53], v[54:57], v[32:35]
	ds_read_b128 v[54:57], v1 offset:8704
	s_waitcnt lgkmcnt(0)
	v_mfma_f32_16x16x32_bf16 v[28:31], v[50:53], v[54:57], v[28:31]
	ds_read_b128 v[54:57], v1 offset:13056
	s_waitcnt lgkmcnt(0)
	v_mfma_f32_16x16x32_bf16 v[24:27], v[50:53], v[54:57], v[24:27]
	ds_read_b128 v[54:57], v1 offset:17408
	s_waitcnt lgkmcnt(0)
	v_mfma_f32_16x16x32_bf16 v[20:23], v[50:53], v[54:57], v[20:23]
	ds_read_b128 v[54:57], v1 offset:21760
	s_waitcnt lgkmcnt(0)
	v_mfma_f32_16x16x32_bf16 v[14:17], v[50:53], v[54:57], v[14:17]
	ds_read_b128 v[54:57], v1 offset:26112
	s_waitcnt lgkmcnt(0)
	v_mfma_f32_16x16x32_bf16 v[10:13], v[50:53], v[54:57], v[10:13]
	ds_read_b128 v[54:57], v1 offset:30464
	s_waitcnt lgkmcnt(0)
	v_mfma_f32_16x16x32_bf16 v[6:9], v[50:53], v[54:57], v[6:9]
.LBB0_1220:
	s_cmp_lt_i32 s1, 64
	s_cbranch_scc1 .LBB0_1222
	v_mov_b32_e32 v45, v3
	v_lshl_add_u64 v[4:5], v[42:43], 0, v[44:45]
	s_waitcnt vmcnt(0)
	v_mov_b64_e32 v[50:51], v[144:145]
	v_mov_b64_e32 v[52:53], v[146:147]
	v_mov_b64_e32 v[54:55], v[140:141]
	v_mov_b64_e32 v[56:57], v[142:143]
	v_or_b32_e32 v1, 64, v48
	v_cmp_le_i32_e32 vcc, v1, v40
	v_or_b32_e32 v4, 0x41, v48
	v_or_b32_e32 v5, 0x42, v48
	v_or_b32_e32 v45, 0x43, v48
	v_or_b32_e32 v49, 0x44, v48
	v_lshlrev_b32_e32 v1, 1, v1
	v_add3_u32 v1, 0, v1, v41
	s_waitcnt vmcnt(0)
	v_cndmask_b32_e32 v2, 0, v54, vcc
	v_cmp_le_i32_e32 vcc, v4, v40
	s_nop 1
	v_cndmask_b32_e32 v4, 0, v55, vcc
	v_cmp_le_i32_e32 vcc, v5, v40
	s_nop 1
	v_cndmask_b32_e32 v5, 0, v56, vcc
	v_cmp_le_i32_e32 vcc, v45, v40
	s_nop 1
	v_cndmask_b32_e32 v45, 0, v57, vcc
	v_cmp_le_i32_e32 vcc, v49, v40
	s_nop 1
	v_cndmask_b32_e32 v49, 0, v50, vcc
	v_or_b32_e32 v50, 0x45, v48
	v_cmp_le_i32_e32 vcc, v50, v40
	v_or_b32_e32 v50, 0x46, v48
	s_nop 0
	v_cndmask_b32_e32 v54, 0, v51, vcc
	v_cmp_le_i32_e32 vcc, v50, v40
	v_or_b32_e32 v50, 0x47, v48
	s_nop 0
	v_cndmask_b32_e32 v55, 0, v52, vcc
	v_cmp_le_i32_e32 vcc, v50, v40
	v_cvt_pk_bf16_f32 v50, v2, v4
	v_cvt_pk_bf16_f32 v51, v5, v45
	v_cvt_pk_bf16_f32 v52, v49, v54
	s_nop 1
	v_cndmask_b32_e32 v53, 0, v53, vcc
	v_cvt_pk_bf16_f32 v53, v55, v53
	ds_read_b128 v[54:57], v1
	s_waitcnt lgkmcnt(0)
	v_mfma_f32_16x16x32_bf16 v[36:39], v[50:53], v[54:57], v[36:39]
	ds_read_b128 v[54:57], v1 offset:4352
	s_waitcnt lgkmcnt(0)
	v_mfma_f32_16x16x32_bf16 v[32:35], v[50:53], v[54:57], v[32:35]
	ds_read_b128 v[54:57], v1 offset:8704
	s_waitcnt lgkmcnt(0)
	v_mfma_f32_16x16x32_bf16 v[28:31], v[50:53], v[54:57], v[28:31]
	ds_read_b128 v[54:57], v1 offset:13056
	s_waitcnt lgkmcnt(0)
	v_mfma_f32_16x16x32_bf16 v[24:27], v[50:53], v[54:57], v[24:27]
	ds_read_b128 v[54:57], v1 offset:17408
	s_waitcnt lgkmcnt(0)
	v_mfma_f32_16x16x32_bf16 v[20:23], v[50:53], v[54:57], v[20:23]
	ds_read_b128 v[54:57], v1 offset:21760
	s_waitcnt lgkmcnt(0)
	v_mfma_f32_16x16x32_bf16 v[14:17], v[50:53], v[54:57], v[14:17]
	ds_read_b128 v[54:57], v1 offset:26112
	s_waitcnt lgkmcnt(0)
	v_mfma_f32_16x16x32_bf16 v[10:13], v[50:53], v[54:57], v[10:13]
	ds_read_b128 v[54:57], v1 offset:30464
	s_waitcnt lgkmcnt(0)
	v_mfma_f32_16x16x32_bf16 v[6:9], v[50:53], v[54:57], v[6:9]
	s_and_b32 s2, s0, -16
	s_cmpk_lt_i32 s1, 0x60
	s_cbranch_scc1 .LBB0_1215
	s_branch .LBB0_1223

.LBB0_1223:
	v_mov_b32_e32 v45, v3
	v_lshl_add_u64 v[4:5], v[42:43], 0, v[44:45]
	s_waitcnt vmcnt(0)
	v_mov_b64_e32 v[42:43], v[152:153]
	v_mov_b64_e32 v[44:45], v[154:155]
	v_mov_b64_e32 v[50:51], v[148:149]
	v_mov_b64_e32 v[52:53], v[150:151]
	v_or_b32_e32 v1, 0x60, v48
	v_cmp_le_i32_e32 vcc, v1, v40
	v_or_b32_e32 v4, 0x61, v48
	v_or_b32_e32 v5, 0x62, v48
	v_or_b32_e32 v49, 0x63, v48
	v_lshlrev_b32_e32 v1, 1, v1
	v_add3_u32 v1, 0, v1, v41
	s_waitcnt vmcnt(0)
	v_cndmask_b32_e32 v2, 0, v50, vcc
	v_cmp_le_i32_e32 vcc, v4, v40
	v_or_b32_e32 v50, 0x64, v48
	s_nop 0
	v_cndmask_b32_e32 v4, 0, v51, vcc
	v_cmp_le_i32_e32 vcc, v5, v40
	s_nop 1
	v_cndmask_b32_e32 v5, 0, v52, vcc
	v_cmp_le_i32_e32 vcc, v49, v40
	s_nop 1
	v_cndmask_b32_e32 v49, 0, v53, vcc
	v_cmp_le_i32_e32 vcc, v50, v40
	s_nop 1
	v_cndmask_b32_e32 v50, 0, v42, vcc
	v_or_b32_e32 v42, 0x65, v48
	v_cmp_le_i32_e32 vcc, v42, v40
	v_or_b32_e32 v42, 0x66, v48
	s_nop 0
	v_cndmask_b32_e32 v51, 0, v43, vcc
	v_cmp_le_i32_e32 vcc, v42, v40
	v_or_b32_e32 v42, 0x67, v48
	s_nop 0
	v_cndmask_b32_e32 v52, 0, v44, vcc
	v_cmp_le_i32_e32 vcc, v42, v40
	v_cvt_pk_bf16_f32 v42, v2, v4
	v_cvt_pk_bf16_f32 v43, v5, v49
	v_cvt_pk_bf16_f32 v44, v50, v51
	s_nop 1
	v_cndmask_b32_e32 v40, 0, v45, vcc
	v_cvt_pk_bf16_f32 v45, v52, v40
	ds_read_b128 v[48:51], v1
	s_waitcnt lgkmcnt(0)
	v_mfma_f32_16x16x32_bf16 v[36:39], v[42:45], v[48:51], v[36:39]
	ds_read_b128 v[48:51], v1 offset:4352
	s_waitcnt lgkmcnt(0)
	v_mfma_f32_16x16x32_bf16 v[32:35], v[42:45], v[48:51], v[32:35]
	ds_read_b128 v[48:51], v1 offset:8704
	s_waitcnt lgkmcnt(0)
	v_mfma_f32_16x16x32_bf16 v[28:31], v[42:45], v[48:51], v[28:31]
	ds_read_b128 v[48:51], v1 offset:13056
	s_waitcnt lgkmcnt(0)
	v_mfma_f32_16x16x32_bf16 v[24:27], v[42:45], v[48:51], v[24:27]
	ds_read_b128 v[48:51], v1 offset:17408
	s_waitcnt lgkmcnt(0)
	v_mfma_f32_16x16x32_bf16 v[20:23], v[42:45], v[48:51], v[20:23]
	ds_read_b128 v[48:51], v1 offset:21760
	s_waitcnt lgkmcnt(0)
	v_mfma_f32_16x16x32_bf16 v[14:17], v[42:45], v[48:51], v[14:17]
	ds_read_b128 v[48:51], v1 offset:26112
	s_waitcnt lgkmcnt(0)
	v_mfma_f32_16x16x32_bf16 v[10:13], v[42:45], v[48:51], v[10:13]
	ds_read_b128 v[48:51], v1 offset:30464
	s_waitcnt lgkmcnt(0)
	v_mfma_f32_16x16x32_bf16 v[6:9], v[42:45], v[48:51], v[6:9]
	s_branch .LBB0_1215

.LBB0_1843:
	s_or_b64 exec, exec, s[0:1]
	s_mov_b32 s2, s73
	v_readlane_b32 s0, v254, 4
	s_waitcnt lgkmcnt(0)
	s_barrier
	v_mov_b32_e32 v2, v0
	v_readlane_b32 s0, v254, 2
	s_nop 0
	v_readlane_b32 s0, v254, 3
	s_nop 0
	v_cmp_gt_i32_e32 vcc, 32, v2
	s_and_saveexec_b64 s[0:1], vcc
	s_cbranch_execz .LBB0_1845
	v_readlane_b32 s4, v254, 15
	v_readlane_b32 s6, v254, 17
	v_readlane_b32 s5, v254, 16
	v_readlane_b32 s7, v254, 18
	s_add_u32 s4, s6, s2
	s_addc_u32 s5, s7, 0
	s_lshl_b64 s[2:3], s[82:83], 8
	s_add_u32 s2, s4, s2
	v_lshlrev_b32_e32 v4, 6, v2
	s_addc_u32 s3, s5, s3
	v_ashrrev_i32_e32 v5, 31, v4
	v_lshl_add_u64 v[4:5], v[4:5], 2, s[2:3]
	v_add_co_u32_e32 v4, vcc, 0x10000, v4
	v_readlane_b32 s2, v254, 26
	s_nop 0
	v_addc_co_u32_e32 v5, vcc, 0, v5, vcc
	global_load_dword v4, v[4:5], off sc1
	v_lshl_add_u32 v5, v2, 2, s2
	s_waitcnt vmcnt(0)
	v_add_u32_e32 v4, 0xff, v4
	v_lshrrev_b32_e32 v4, 8, v4
	ds_write_b32 v5, v4 offset:132
	v_mov_b32_e32 v6, v4
	s_nop 1
	v_add_u32_dpp v6, v6, v6 row_shr:1 row_mask:0xf bank_mask:0xf
	s_nop 1
	v_add_u32_dpp v6, v6, v6 row_shr:2 row_mask:0xf bank_mask:0xf
	s_nop 1
	v_add_u32_dpp v6, v6, v6 row_shr:4 row_mask:0xf bank_mask:0xf
	s_nop 1
	v_add_u32_dpp v6, v6, v6 row_shr:8 row_mask:0xf bank_mask:0xf
	s_nop 1
	v_add_u32_dpp v6, v6, v6 row_bcast:15 row_mask:0xa bank_mask:0xf
	ds_write_b32 v5, v6 offset:4
	v_sub_u32_e32 v7, v6, v4
	ds_write_b32 v5, v7
.LBB0_1845:
	s_or_b64 exec, exec, s[0:1]
	v_cmp_eq_u32_e32 vcc, 0, v2
	s_waitcnt lgkmcnt(0)
	s_barrier
	s_and_saveexec_b64 s[0:1], vcc
	s_branch .LBB0_1847

.LBB0_1849:
	s_andn2_b64 vcc, exec, s[8:9]
	s_mov_b64 s[12:13], 0
	s_cbranch_vccnz .LBB0_1854
	s_sub_i32 s6, 3, s55
	s_lshr_b32 s6, s0, s6
	v_readlane_b32 s1, v254, 51
	v_and_b32_e32 v4, 63, v0
	s_nop 0
	v_lshl_add_u32 v4, v4, 2, s1
	ds_read_b32 v4, v4
	s_waitcnt lgkmcnt(0)
	v_cmp_ge_i32_e64 s[100:101], s6, v4
	s_nop 3
	s_and_b32 s100, s100, 0x7fffffff
	s_bcnt1_i32_b32 s1, s100
	s_lshl_b32 s7, s1, 2
	s_add_i32 s7, s7, 0
	s_add_i32 s7, s7, 0x23400
	v_mov_b32_e32 v2, s7
	ds_read_b32 v2, v2
	s_lshl_b32 s8, s1, 6
	s_waitcnt lgkmcnt(0)
	v_sub_u32_e32 v2, s6, v2
	s_nop 0
	v_readfirstlane_b32 s7, v2
	s_add_i32 s8, s7, s8
	s_mul_i32 s7, s6, s3
	s_sub_i32 s7, s0, s7
	s_mul_i32 s0, s1, s3
	s_add_i32 s10, s0, s7
	s_branch .LBB0_1855

.LBB0_1859:
	global_load_dword v2, v3, s[0:1] sc1
	s_mov_b64 s[12:13], -1
	s_waitcnt vmcnt(0)
	v_readfirstlane_b32 s11, v2
	s_cmp_gt_u32 s11, 63
	s_cbranch_scc1 .LBB0_1858
	s_sleep 2
	global_load_dword v2, v3, s[0:1] sc1
	s_waitcnt vmcnt(0)
	v_readfirstlane_b32 s11, v2
	s_cmp_lt_u32 s11, 64
	s_cbranch_scc0 .LBB0_1858
	s_sleep 2
	global_load_dword v2, v3, s[0:1] sc1
	s_waitcnt vmcnt(0)
	v_readfirstlane_b32 s11, v2
	s_cmp_lt_u32 s11, 64
	s_cbranch_scc0 .LBB0_1858
	s_sleep 2
	global_load_dword v2, v3, s[0:1] sc1
	s_waitcnt vmcnt(0)
	v_readfirstlane_b32 s11, v2
	s_cmp_lt_u32 s11, 64
	s_cbranch_scc0 .LBB0_1858
	s_sleep 2
	global_load_dword v2, v3, s[0:1] sc1
	s_waitcnt vmcnt(0)
	v_readfirstlane_b32 s11, v2
	s_cmp_lt_u32 s11, 64
	s_cbranch_scc0 .LBB0_1858
	s_add_i32 s9, s9, -5
	s_cmp_eq_u32 s9, 0
	s_cselect_b64 s[12:13], -1, 0
	s_sleep 2
	s_branch .LBB0_1858
.LBB0_1866:
	buffer_inv sc1
	s_waitcnt vmcnt(0)
